# attention work-queue dequeue: the prefetched unit index is used without draining the previous unit's output stores (no vmcnt(0) on the prefetch path)
# baseline (speedup 1.0000x reference)
.Lpf_gqa_use:
	v_mov_b32_e32 v3, v250
	s_or_b64 exec, exec, s[40:41]
	s_branch .Lpf_gqa_nw

.Lpf_gqa_nw:
	v_readfirstlane_b32 s2, v3
	v_mov_b32_e32 v3, s92
	s_nop 0
	v_add_u32_e32 v2, s2, v2
	ds_write_b32 v3, v2
	global_atomic_add v250, v211, v1, s[24:25] sc0
	s_mov_b32 s99, 1

.Lpf_diff_nw:
	v_readfirstlane_b32 s2, v3
	v_mov_b32_e32 v3, s92
	s_nop 0
	v_add_u32_e32 v2, s2, v2
	ds_write_b32 v3, v2
	global_atomic_add v250, v211, v1, s[24:25] offset:256 sc0
	s_mov_b32 s99, 1
